# baseline (speedup 1.0000x reference)
.LBB0_58:
	s_and_b64 s[4:5], s[30:31], exec
	s_cselect_b32 s5, s21, s23
	s_cselect_b32 s4, s20, s22
	s_or_b32 s6, s34, s33
	s_mulk_i32 s6, 0x880
	s_add_u32 s4, s4, s6
	s_addc_u32 s5, s5, 0
	v_lshlrev_b32_e32 v38, 1, v34
	v_mov_b32_e32 v39, 0
	s_waitcnt vmcnt(0)
	v_cvt_pk_f16_f32 v10, v10, v11
	v_cvt_pk_f16_f32 v11, v12, v13
	global_store_dwordx2 v38, v[10:11], s[4:5] sc0 sc1
	v_cvt_pk_f16_f32 v10, v18, v19
	ds_read_b32 v18, v39 offset:32
	v_lshl_add_u64 v[40:41], s[4:5], 0, v[38:39]
	s_movk_i32 s6, 0x1000
	v_cvt_pk_f16_f32 v11, v20, v21
	v_add_co_u32_e32 v12, vcc, s6, v40
	global_store_dwordx2 v38, v[10:11], s[4:5] offset:2176 sc0 sc1
	v_cvt_pk_f16_f32 v10, v30, v31
	v_cvt_pk_f16_f32 v11, v32, v33
	v_addc_co_u32_e32 v13, vcc, 0, v41, vcc
	global_store_dwordx2 v[12:13], v[10:11], off offset:256 sc0 sc1
	v_cvt_pk_f16_f32 v10, v22, v23
	v_cvt_pk_f16_f32 v11, v24, v25
	s_waitcnt lgkmcnt(0)
	v_cmp_gt_i32_e32 vcc, 0, v18
	global_store_dwordx2 v[12:13], v[10:11], off offset:2432 sc0 sc1
	s_and_b64 vcc, exec, vcc
	v_mov_b32_e32 v13, 0
	v_mov_b32_e32 v12, 0
	v_mov_b32_e32 v11, 0
	v_mov_b32_e32 v10, 0
	s_cbranch_vccnz .LBB0_60
	v_mov_b32_e32 v19, 0
	v_lshlrev_b64 v[10:11], 12, v[18:19]
	v_lshl_add_u64 v[10:11], v[36:37], 0, v[10:11]
	global_load_dwordx4 v[10:13], v[10:11], off nt

.LBB0_66:
	v_cvt_pk_f16_f32 v6, v6, v7
	v_cvt_pk_f16_f32 v7, v8, v9
	v_mov_b32_e32 v9, 0
	v_mov_b32_e32 v8, v38
	v_lshl_add_u64 v[40:41], s[4:5], 0, v[8:9]
	v_add_co_u32_e32 v42, vcc, 0x2000, v40
	v_cvt_pk_f16_f32 v2, v2, v3
	s_nop 0
	v_addc_co_u32_e32 v43, vcc, 0, v41, vcc
	v_cvt_pk_f16_f32 v3, v4, v5
	global_store_dwordx2 v[42:43], v[2:3], off offset:2688 sc0 sc1
	ds_read_b32 v2, v9 offset:48
	global_store_dwordx2 v[42:43], v[6:7], off offset:512 sc0 sc1
	v_add_co_u32_e32 v6, vcc, 0x3000, v40
	v_cvt_pk_f16_f32 v4, v26, v27
	s_nop 0
	v_addc_co_u32_e32 v7, vcc, 0, v41, vcc
	v_cvt_pk_f16_f32 v5, v28, v29
	s_waitcnt lgkmcnt(0)
	v_cmp_gt_i32_e32 vcc, 0, v2
	global_store_dwordx2 v[6:7], v[4:5], off offset:768 sc0 sc1
	v_cvt_pk_f16_f32 v4, v14, v15
	v_cvt_pk_f16_f32 v5, v16, v17
	s_and_b64 vcc, exec, vcc
	v_mov_b32_e32 v17, 0
	v_mov_b32_e32 v16, 0
	v_mov_b32_e32 v15, 0
	v_mov_b32_e32 v14, 0
	global_store_dwordx2 v[6:7], v[4:5], off offset:2944 sc0 sc1
	s_cbranch_vccnz .LBB0_68
	v_mov_b32_e32 v3, 0
	v_lshlrev_b64 v[2:3], 12, v[2:3]
	v_lshl_add_u64 v[2:3], v[36:37], 0, v[2:3]
	global_load_dwordx4 v[14:17], v[2:3], off nt

.LBB0_74:
	s_waitcnt vmcnt(4)
	v_cvt_pk_f16_f32 v10, v10, v11
	v_cvt_pk_f16_f32 v11, v12, v13
	v_mov_b32_e32 v13, 0
	v_mov_b32_e32 v12, v38
	v_lshl_add_u64 v[12:13], s[4:5], 0, v[12:13]
	v_add_co_u32_e32 v36, vcc, 0x4000, v12
	s_waitcnt vmcnt(0)
	v_cvt_pk_f16_f32 v6, v6, v7
	v_addc_co_u32_e32 v37, vcc, 0, v13, vcc
	global_store_dwordx2 v[36:37], v[10:11], off offset:1024 sc0 sc1
	v_cvt_pk_f16_f32 v10, v18, v19
	v_cvt_pk_f16_f32 v11, v20, v39
	v_add_co_u32_e32 v18, vcc, 0x5000, v12
	global_store_dwordx2 v[36:37], v[10:11], off offset:3200 sc0 sc1
	v_cvt_pk_f16_f32 v10, v30, v31
	v_cvt_pk_f16_f32 v11, v32, v33
	v_addc_co_u32_e32 v19, vcc, 0, v13, vcc
	global_store_dwordx2 v[18:19], v[10:11], off offset:1280 sc0 sc1
	v_cvt_pk_f16_f32 v10, v22, v23
	v_cvt_pk_f16_f32 v11, v24, v25
	global_store_dwordx2 v[18:19], v[10:11], off offset:3456 sc0 sc1
	v_cvt_pk_f16_f32 v10, v14, v15
	v_add_co_u32_e32 v14, vcc, 0x6000, v12
	v_cvt_pk_f16_f32 v7, v8, v9
	s_nop 0
	v_addc_co_u32_e32 v15, vcc, 0, v13, vcc
	v_add_co_u32_e32 v8, vcc, 0x7000, v12
	v_cvt_pk_f16_f32 v11, v16, v17
	global_store_dwordx2 v[14:15], v[6:7], off offset:3712 sc0 sc1
	v_cvt_pk_f16_f32 v6, v26, v27
	v_cvt_pk_f16_f32 v7, v28, v29
	v_addc_co_u32_e32 v9, vcc, 0, v13, vcc
	global_store_dwordx2 v[14:15], v[10:11], off offset:1536 sc0 sc1
	global_store_dwordx2 v[8:9], v[6:7], off offset:1792 sc0 sc1
	v_cvt_pk_f16_f32 v2, v2, v3
	s_mov_b64 s[6:7], -1
	s_and_b64 vcc, exec, s[28:29]
	s_cbranch_vccz .LBB0_76
.LBB0_75:
	s_load_dwordx2 s[6:7], s[0:1], 0x0
	s_lshl_b32 s4, s2, 4
	s_mov_b32 s5, 0
	s_addk_i32 s4, 0xd400
	s_lshl_b64 s[8:9], s[4:5], 12
	s_waitcnt lgkmcnt(0)
	s_add_u32 s6, s6, s8
	v_mov_b32_e32 v35, 0
	s_addc_u32 s7, s7, s9
	v_lshlrev_b32_e32 v2, 4, v0
	v_mov_b32_e32 v3, v35
	v_lshl_add_u64 v[52:53], s[6:7], 0, v[2:3]
	s_movk_i32 s8, 0x2000
	global_load_dwordx4 v[6:9], v2, s[6:7] nt
	v_add_co_u32_e32 v2, vcc, s8, v52
	s_movk_i32 s9, 0x4000
	s_nop 0
	v_addc_co_u32_e32 v3, vcc, 0, v53, vcc
	global_load_dwordx4 v[10:13], v[2:3], off offset:-4096 nt
	global_load_dwordx4 v[14:17], v[2:3], off nt
	v_add_co_u32_e32 v2, vcc, s9, v52
	s_movk_i32 s10, 0x6000
	s_nop 0
	v_addc_co_u32_e32 v3, vcc, 0, v53, vcc
	global_load_dwordx4 v[18:21], v[2:3], off offset:-4096 nt
	global_load_dwordx4 v[22:25], v[2:3], off nt
	v_add_co_u32_e32 v2, vcc, s10, v52
	s_mov_b32 s5, 0x8000
	s_nop 0
	v_addc_co_u32_e32 v3, vcc, 0, v53, vcc
	global_load_dwordx4 v[26:29], v[2:3], off offset:-4096 nt
	global_load_dwordx4 v[30:33], v[2:3], off nt
	v_add_co_u32_e32 v2, vcc, s5, v52
	s_mov_b32 s11, 0xa000
	s_nop 0
	v_addc_co_u32_e32 v3, vcc, 0, v53, vcc
	global_load_dwordx4 v[36:39], v[2:3], off offset:-4096 nt
	global_load_dwordx4 v[40:43], v[2:3], off nt
	v_add_co_u32_e32 v2, vcc, s11, v52
	s_mov_b32 s12, 0xc000
	s_nop 0
	v_addc_co_u32_e32 v3, vcc, 0, v53, vcc
	v_add_co_u32_e32 v56, vcc, s12, v52
	s_mov_b32 s14, 0xf000
	s_nop 0
	v_addc_co_u32_e32 v57, vcc, 0, v53, vcc
	global_load_dwordx4 v[44:47], v[2:3], off offset:-4096 nt
	global_load_dwordx4 v[48:51], v[2:3], off nt
	v_add_co_u32_e32 v2, vcc, s14, v52
	s_mov_b32 s13, 0xe000
	s_nop 0
	v_addc_co_u32_e32 v3, vcc, 0, v53, vcc
	v_add_co_u32_e32 v52, vcc, s13, v52
	global_load_dwordx4 v[2:5], v[2:3], off nt
	s_nop 0
	v_addc_co_u32_e32 v53, vcc, 0, v53, vcc
	s_load_dwordx2 s[6:7], s[0:1], 0x40
	s_mul_hi_u32 s15, s4, 0x880
	s_mulk_i32 s4, 0x880
	v_lshlrev_b32_e32 v54, 3, v0
	v_mov_b32_e32 v55, v35
	s_waitcnt lgkmcnt(0)
	s_add_u32 s4, s6, s4
	s_addc_u32 s5, s7, s15
	s_movk_i32 s6, 0x1000
	s_movk_i32 s7, 0x3000
	s_movk_i32 s11, 0x5000
	v_lshlrev_b32_e32 v34, 2, v0
	s_waitcnt vmcnt(11)
	v_cvt_pk_f16_f32 v58, v6, v7
	v_cvt_pk_f16_f32 v59, v8, v9
	global_load_dwordx4 v[6:9], v[56:57], off offset:-4096 nt
	s_waitcnt vmcnt(11)
	v_cvt_pk_f16_f32 v60, v10, v11
	v_cvt_pk_f16_f32 v61, v12, v13
	global_load_dwordx4 v[10:13], v[56:57], off nt
	s_waitcnt vmcnt(11)
	v_cvt_pk_f16_f32 v62, v14, v15
	v_cvt_pk_f16_f32 v63, v16, v17
	global_load_dwordx4 v[14:17], v[52:53], off offset:-4096 nt
	s_waitcnt vmcnt(11)
	v_cvt_pk_f16_f32 v56, v18, v19
	v_cvt_pk_f16_f32 v57, v20, v21
	global_load_dwordx4 v[18:21], v[52:53], off nt
	v_lshl_add_u64 v[52:53], s[4:5], 0, v[54:55]
	global_store_dwordx2 v54, v[58:59], s[4:5] sc0 sc1
	global_store_dwordx2 v54, v[60:61], s[4:5] offset:2176 sc0 sc1
	v_add_co_u32_e32 v54, vcc, s6, v52
	s_waitcnt vmcnt(13)
	v_cvt_pk_f16_f32 v22, v22, v23
	v_addc_co_u32_e32 v55, vcc, 0, v53, vcc
	v_cvt_pk_f16_f32 v23, v24, v25
	v_add_co_u32_e32 v24, vcc, s8, v52
	global_store_dwordx2 v[54:55], v[62:63], off offset:256 sc0 sc1
	global_store_dwordx2 v[54:55], v[56:57], off offset:2432 sc0 sc1
	v_addc_co_u32_e32 v25, vcc, 0, v53, vcc
	global_store_dwordx2 v[24:25], v[22:23], off offset:512 sc0 sc1
	s_waitcnt vmcnt(15)
	v_cvt_pk_f16_f32 v22, v26, v27
	v_cvt_pk_f16_f32 v23, v28, v29
	global_store_dwordx2 v[24:25], v[22:23], off offset:2688 sc0 sc1
	v_add_co_u32_e32 v24, vcc, s7, v52
	s_waitcnt vmcnt(15)
	v_cvt_pk_f16_f32 v22, v30, v31
	v_cvt_pk_f16_f32 v23, v32, v33
	v_addc_co_u32_e32 v25, vcc, 0, v53, vcc
	global_store_dwordx2 v[24:25], v[22:23], off offset:768 sc0 sc1
	s_waitcnt vmcnt(15)
	v_cvt_pk_f16_f32 v22, v36, v37
	v_cvt_pk_f16_f32 v23, v38, v39
	global_store_dwordx2 v[24:25], v[22:23], off offset:2944 sc0 sc1
	v_add_co_u32_e32 v24, vcc, s9, v52
	s_waitcnt vmcnt(15)
	v_cvt_pk_f16_f32 v22, v40, v41
	v_cvt_pk_f16_f32 v23, v42, v43
	v_addc_co_u32_e32 v25, vcc, 0, v53, vcc
	global_store_dwordx2 v[24:25], v[22:23], off offset:1024 sc0 sc1
	s_waitcnt vmcnt(15)
	v_cvt_pk_f16_f32 v22, v44, v45
	v_cvt_pk_f16_f32 v23, v46, v47
	global_store_dwordx2 v[24:25], v[22:23], off offset:3200 sc0 sc1
	v_add_co_u32_e32 v24, vcc, s11, v52
	s_waitcnt vmcnt(15)
	v_cvt_pk_f16_f32 v22, v48, v49
	v_addc_co_u32_e32 v25, vcc, 0, v53, vcc
	v_cvt_pk_f16_f32 v23, v50, v51
	s_waitcnt vmcnt(14)
	v_cvt_pk_f16_f32 v2, v2, v3
	s_mov_b64 s[6:7], -1
	global_store_dwordx2 v[24:25], v[22:23], off offset:1280 sc0 sc1
	s_waitcnt vmcnt(14)
	v_cvt_pk_f16_f32 v6, v6, v7
	v_cvt_pk_f16_f32 v7, v8, v9
	v_add_co_u32_e32 v8, vcc, s10, v52
	global_store_dwordx2 v[24:25], v[6:7], off offset:3456 sc0 sc1
	s_waitcnt vmcnt(14)
	v_cvt_pk_f16_f32 v6, v10, v11
	v_cvt_pk_f16_f32 v7, v12, v13
	v_addc_co_u32_e32 v9, vcc, 0, v53, vcc
	global_store_dwordx2 v[8:9], v[6:7], off offset:1536 sc0 sc1
	s_waitcnt vmcnt(14)
	v_cvt_pk_f16_f32 v6, v14, v15
	v_cvt_pk_f16_f32 v7, v16, v17
	global_store_dwordx2 v[8:9], v[6:7], off offset:3712 sc0 sc1
	v_add_co_u32_e32 v8, vcc, 0x7000, v52
	s_waitcnt vmcnt(14)
	v_cvt_pk_f16_f32 v6, v18, v19
	v_cvt_pk_f16_f32 v7, v20, v21
	v_addc_co_u32_e32 v9, vcc, 0, v53, vcc
	global_store_dwordx2 v[8:9], v[6:7], off offset:1792 sc0 sc1

.LBB0_77:
	s_load_dwordx4 s[4:7], s[0:1], 0x20
	s_load_dwordx2 s[8:9], s[0:1], 0x30
	s_lshl_b32 s2, s2, 4
	s_lshr_b32 s10, s3, 6
	s_and_b32 s11, s2, 0x3f0
	s_cmp_eq_u32 s10, 1
	s_waitcnt lgkmcnt(0)
	s_cselect_b32 s2, s6, s8
	s_cselect_b32 s6, s7, s9
	s_cmp_lt_u32 s3, 64
	s_cselect_b32 s3, s5, s6
	s_cselect_b32 s2, s4, s2
	s_lshl_b32 s4, s11, 12
	s_add_u32 s2, s2, s4
	v_mov_b32_e32 v35, 0
	s_addc_u32 s3, s3, 0
	v_lshlrev_b32_e32 v2, 4, v0
	v_mov_b32_e32 v3, v35
	v_lshl_add_u64 v[52:53], s[2:3], 0, v[2:3]
	s_movk_i32 s6, 0x2000
	global_load_dwordx4 v[6:9], v2, s[2:3] nt
	v_add_co_u32_e32 v2, vcc, s6, v52
	s_movk_i32 s7, 0x4000
	s_nop 0
	v_addc_co_u32_e32 v3, vcc, 0, v53, vcc
	global_load_dwordx4 v[10:13], v[2:3], off offset:-4096 nt
	global_load_dwordx4 v[14:17], v[2:3], off nt
	v_add_co_u32_e32 v2, vcc, s7, v52
	s_movk_i32 s8, 0x6000
	s_nop 0
	v_addc_co_u32_e32 v3, vcc, 0, v53, vcc
	global_load_dwordx4 v[18:21], v[2:3], off offset:-4096 nt
	global_load_dwordx4 v[22:25], v[2:3], off nt
	v_add_co_u32_e32 v2, vcc, s8, v52
	s_mov_b32 s4, 0x8000
	s_nop 0
	v_addc_co_u32_e32 v3, vcc, 0, v53, vcc
	global_load_dwordx4 v[26:29], v[2:3], off offset:-4096 nt
	global_load_dwordx4 v[30:33], v[2:3], off nt
	v_add_co_u32_e32 v2, vcc, s4, v52
	s_mov_b32 s5, 0xa000
	s_nop 0
	v_addc_co_u32_e32 v3, vcc, 0, v53, vcc
	global_load_dwordx4 v[36:39], v[2:3], off offset:-4096 nt
	global_load_dwordx4 v[40:43], v[2:3], off nt
	v_add_co_u32_e32 v2, vcc, s5, v52
	s_mov_b32 s9, 0xc000
	s_nop 0
	v_addc_co_u32_e32 v3, vcc, 0, v53, vcc
	v_add_co_u32_e32 v54, vcc, s9, v52
	s_mov_b32 s13, 0xf000
	s_nop 0
	v_addc_co_u32_e32 v55, vcc, 0, v53, vcc
	global_load_dwordx4 v[44:47], v[2:3], off offset:-4096 nt
	global_load_dwordx4 v[48:51], v[2:3], off nt
	v_add_co_u32_e32 v2, vcc, s13, v52
	s_mov_b32 s12, 0xe000
	s_nop 0
	v_addc_co_u32_e32 v3, vcc, 0, v53, vcc
	v_add_co_u32_e32 v52, vcc, s12, v52
	global_load_dwordx4 v[2:5], v[2:3], off nt
	s_nop 0
	v_addc_co_u32_e32 v53, vcc, 0, v53, vcc
	s_load_dwordx2 s[0:1], s[0:1], 0x58
	s_lshl_b32 s2, s10, 10
	s_or_b32 s2, s2, s11
	s_mov_b32 s3, 0
	s_mulk_i32 s2, 0x440
	s_lshl_b64 s[2:3], s[2:3], 1
	s_waitcnt lgkmcnt(0)
	s_add_u32 s4, s0, s2
	v_lshlrev_b32_e32 v34, 2, v0
	v_lshlrev_b32_e32 v0, 3, v0
	s_addc_u32 s5, s1, s3
	v_mov_b32_e32 v1, v35
	s_movk_i32 s0, 0x1000
	s_movk_i32 s1, 0x3000
	s_movk_i32 s2, 0x5000
	s_waitcnt vmcnt(11)
	v_cvt_pk_f16_f32 v56, v6, v7
	v_cvt_pk_f16_f32 v57, v8, v9
	global_load_dwordx4 v[6:9], v[54:55], off offset:-4096 nt
	s_waitcnt vmcnt(11)
	v_cvt_pk_f16_f32 v58, v10, v11
	v_cvt_pk_f16_f32 v59, v12, v13
	global_load_dwordx4 v[10:13], v[54:55], off nt
	s_waitcnt vmcnt(11)
	v_cvt_pk_f16_f32 v60, v14, v15
	v_cvt_pk_f16_f32 v61, v16, v17
	global_load_dwordx4 v[14:17], v[52:53], off offset:-4096 nt
	s_waitcnt vmcnt(11)
	v_cvt_pk_f16_f32 v18, v18, v19
	global_load_dwordx4 v[52:55], v[52:53], off nt
	v_cvt_pk_f16_f32 v19, v20, v21
	global_store_dwordx2 v0, v[56:57], s[4:5] sc0 sc1
	global_store_dwordx2 v0, v[58:59], s[4:5] offset:2176 sc0 sc1
	v_lshl_add_u64 v[0:1], s[4:5], 0, v[0:1]
	v_add_co_u32_e32 v56, vcc, s0, v0
	s_waitcnt vmcnt(6)
	v_cvt_pk_f16_f32 v2, v2, v3
	v_addc_co_u32_e32 v57, vcc, 0, v1, vcc
	v_add_co_u32_e32 v20, vcc, s6, v0
	global_store_dwordx2 v[56:57], v[18:19], off offset:2432 sc0 sc1
	v_cvt_pk_f16_f32 v18, v22, v23
	v_cvt_pk_f16_f32 v19, v24, v25
	v_addc_co_u32_e32 v21, vcc, 0, v1, vcc
	global_store_dwordx2 v[20:21], v[18:19], off offset:512 sc0 sc1
	v_cvt_pk_f16_f32 v18, v26, v27
	v_cvt_pk_f16_f32 v19, v28, v29
	global_store_dwordx2 v[20:21], v[18:19], off offset:2688 sc0 sc1
	v_add_co_u32_e32 v20, vcc, s1, v0
	v_cvt_pk_f16_f32 v18, v30, v31
	v_cvt_pk_f16_f32 v19, v32, v33
	v_addc_co_u32_e32 v21, vcc, 0, v1, vcc
	global_store_dwordx2 v[20:21], v[18:19], off offset:768 sc0 sc1
	v_cvt_pk_f16_f32 v18, v36, v37
	v_cvt_pk_f16_f32 v19, v38, v39
	global_store_dwordx2 v[20:21], v[18:19], off offset:2944 sc0 sc1
	v_add_co_u32_e32 v20, vcc, s7, v0
	v_cvt_pk_f16_f32 v18, v40, v41
	v_cvt_pk_f16_f32 v19, v42, v43
	v_addc_co_u32_e32 v21, vcc, 0, v1, vcc
	global_store_dwordx2 v[20:21], v[18:19], off offset:1024 sc0 sc1
	v_cvt_pk_f16_f32 v18, v44, v45
	v_cvt_pk_f16_f32 v19, v46, v47
	global_store_dwordx2 v[20:21], v[18:19], off offset:3200 sc0 sc1
	v_add_co_u32_e32 v20, vcc, s2, v0
	v_cvt_pk_f16_f32 v18, v48, v49
	s_nop 0
	v_addc_co_u32_e32 v21, vcc, 0, v1, vcc
	s_waitcnt vmcnt(12)
	v_cvt_pk_f16_f32 v6, v6, v7
	v_cvt_pk_f16_f32 v7, v8, v9
	v_add_co_u32_e32 v8, vcc, s8, v0
	global_store_dwordx2 v[20:21], v[6:7], off offset:3456 sc0 sc1
	s_waitcnt vmcnt(12)
	v_cvt_pk_f16_f32 v6, v10, v11
	v_cvt_pk_f16_f32 v7, v12, v13
	v_addc_co_u32_e32 v9, vcc, 0, v1, vcc
	global_store_dwordx2 v[8:9], v[6:7], off offset:1536 sc0 sc1
	s_waitcnt vmcnt(12)
	v_cvt_pk_f16_f32 v6, v14, v15
	v_cvt_pk_f16_f32 v7, v16, v17
	v_add_co_u32_e32 v0, vcc, 0x7000, v0
	v_cvt_pk_f16_f32 v19, v50, v51
	global_store_dwordx2 v[8:9], v[6:7], off offset:3712 sc0 sc1
	s_waitcnt vmcnt(12)
	v_cvt_pk_f16_f32 v6, v52, v53
	v_cvt_pk_f16_f32 v7, v54, v55
	v_addc_co_u32_e32 v1, vcc, 0, v1, vcc
	s_mov_b64 s[6:7], -1
	global_store_dwordx2 v[56:57], v[60:61], off offset:256 sc0 sc1
	global_store_dwordx2 v[20:21], v[18:19], off offset:1280 sc0 sc1
	global_store_dwordx2 v[0:1], v[6:7], off offset:1792 sc0 sc1

.LBB0_80:
	v_lshl_add_u64 v[0:1], v[34:35], 1, s[4:5]
	v_add_co_u32_e32 v0, vcc, 0x7000, v0
	v_cvt_pk_f16_f32 v3, v4, v5
	s_nop 0
	v_addc_co_u32_e32 v1, vcc, 0, v1, vcc
	global_store_dwordx2 v[0:1], v[2:3], off offset:3968 sc0 sc1
	s_endpgm
